# v41 stack + layer-0 gate/up GEMM unit-boundary hosting of list conversion items (half of workgroups per boundary)
# baseline (speedup 1.0000x reference)
; #define LAS __attribute__((address_space(3)))
; __device__ __forceinline__ void f8w_bar_flush(Frame& F, volatile LAS unsigned* st, int upto) {
;     if (F.wave == 0) return;
;     const int wv = F.wave, wi = (int)blockIdx.x * 7 + wv - 1; int i = (int)st[8 + wv];
;     if (upto > F8W_BARQ0) upto = f8w_bar_count(wi);
;     if (i >= upto) return;
;     for (; i < upto; ++i) f8w_convert_one(F, f8w_bar_item(wi, i));
;     if (F.lane == 0) st[8 + wv] = (unsigned)upto;
; }
.Lfl_entry:
	v_readlane_b32 s0, v254, 8
	v_readlane_b32 s1, v254, 9
	v_mov_b32_e32 v2, v0
	v_writelane_b32 v254, s0, 8
	s_nop 1
	v_writelane_b32 v254, s1, 9
	s_movk_i32 s0, 0x100
	s_nop 0
	v_readfirstlane_b32 s0, v2
	s_ashr_i32 s89, s0, 6
	s_cmp_lt_u32 s0, 64
	v_and_b32_e32 v186, 63, v2
	s_cbranch_scc1 .LBB0_1525
	v_readlane_b32 s0, v254, 14
	s_add_i32 s8, s89, s0
	s_lshl_b32 s0, s89, 2
	s_add_i32 s4, s0, 0
	s_add_i32 s4, s4, 0x20160
	v_mov_b32_e32 v1, s4
	ds_read_b32 v1, v1 offset:32
	v_readlane_b32 s0, v254, 57
	s_cmpk_gt_i32 s8, 0x380
	v_readlane_b32 s1, v254, 58
	s_cselect_b32 s2, 23, 20
	s_and_b64 s[0:1], s[0:1], exec
	s_cselect_b32 s5, 15, s2
	s_waitcnt lgkmcnt(0)
	v_readfirstlane_b32 s6, v1
	s_cmp_lg_u32 s100, 0x1234
	s_cbranch_scc1 .Lfl_noovr
	s_add_u32 s5, s6, 1
	s_min_u32 s5, s5, s2
.Lfl_noovr:
	v_cmp_le_i32_e32 vcc, s5, v1
	s_cbranch_vccnz .LBB0_1525
	s_cmpk_gt_i32 s8, 0x380
	s_cselect_b64 s[0:1], -1, 0
	s_add_i32 s7, s8, 0x9bff
	s_addk_i32 s8, 0x1aff
	s_add_u32 s9, s80, 0x41400000
	s_addc_u32 s10, s81, 0
	s_add_u32 s11, s80, 0x2b400000
	v_readlane_b32 s2, v254, 32
	v_lshlrev_b32_e32 v1, 2, v2
	v_and_b32_e32 v72, 48, v2
	s_addc_u32 s12, s81, 0
	s_add_i32 s2, s2, s89
	s_mul_i32 s3, s6, 0x380
	v_and_b32_e32 v1, 60, v1
	v_lshlrev_b32_e32 v73, 12, v72
	s_add_i32 s13, s2, s3
	s_branch .LBB0_1512

; #define LAS __attribute__((address_space(3)))
; __device__ __forceinline__ unsigned xb_ld(unsigned* p)              { return __hip_atomic_load(p, __ATOMIC_RELAXED, __HIP_MEMORY_SCOPE_AGENT); }
; __device__ __forceinline__ unsigned xb_add(unsigned* p, unsigned v) { return __hip_atomic_fetch_add(p, v, __ATOMIC_RELAXED, __HIP_MEMORY_SCOPE_AGENT); }
; #define XB_SPIN(cond, bar) do { unsigned _sp = 0; while (cond) { __builtin_amdgcn_s_sleep(1); \
;     if ((++_sp & 255u) == 0u) { if (xb_ld(&(bar)[XB_TMO])) break; if (_sp > XB_SPIN_CAP) { atomicAdd(&(bar)[XB_TMO], 1u); break; } } } } while (0)
; #define SEAM(k) do { if (IN(k) && IN((k) + 1)) { for (int br_ = 0; br_ < BARREP; ++br_) { XcdBarrier b2 = bar; asm volatile("" : "+s"(b2.bar), "+s"(b2.x)); \
;         if (hostbar && (k) >= 1 && (k) <= 2 + PH_PER_LAYER + 5) xcd_barrier_host(b2, F, (unsigned)(k) + 1u); else xcd_barrier(b2); } } } while (0)
; __device__ __forceinline__ void xcd_barrier_host(const XcdBarrier& b, Frame& F, unsigned epoch) {
;     asm volatile("s_waitcnt vmcnt(0)" ::: "memory");
;     __syncthreads();
;     volatile LAS unsigned* st = b.st;
;     if (F.wave == 0) {
;       if (threadIdx.x == 0) {
;         unsigned* bar = b.bar;
;         __builtin_amdgcn_s_waitcnt(0);
;         unsigned nloc = b.st[0], nx = b.st[1];
;         if (nloc == 0u) { xcd_barrier_complete(bar, b.x, nloc, nx); b.st[0] = nloc; b.st[1] = nx; }
;         const unsigned old = xb_add(&bar[XB_XSUB(b.x)], 1u);
;         const unsigned gen = old / nloc;
;         if (old + 1u == (gen + 1u) * nloc) {
;             __builtin_amdgcn_fence(__ATOMIC_RELEASE, "agent");
;             asm volatile("s_waitcnt vmcnt(0)" ::: "memory");
;             const unsigned og = xb_add(&bar[XB_TOP], 1u);
;             const unsigned tg = og / nx;
;             if (og + 1u == (tg + 1u) * nx) xb_add(&bar[XB_TOPGEN], 1u);
;             else XB_SPIN(xb_ld(&bar[XB_TOPGEN]) == tg, bar);
; __global__ void __launch_bounds__(NTHR, 2) fwd_kernel(Args args) {
;     ...
;         if (hostbar) { frame_fence(F); f8w_bar_flush(F, bar.st, l == 0 ? F8W_BARQ0 : F8W_BARQ0 + F8W_BARQ); }
;         SEAM(pb + 6);
.LBB0_1525:
	s_cmp_eq_u32 s100, 0x1234
	s_cbranch_scc1 .Lh_return
	s_mul_i32 s0, s54, 10
	s_add_i32 s38, s0, 9
	s_cmp_lt_i32 s38, s87
	s_cselect_b64 s[34:35], -1, 0
	s_and_b64 s[0:1], s[24:25], s[34:35]
	s_andn2_b64 vcc, exec, s[0:1]
	s_cbranch_vccnz .LBB0_1645
	v_readlane_b32 s0, v254, 12
	v_readlane_b32 s2, v254, 57
	v_readlane_b32 s1, v254, 13
	v_readlane_b32 s3, v254, 58
	s_and_b64 s[0:1], s[0:1], s[2:3]
	v_readlane_b32 s36, v254, 5
	v_readlane_b32 s37, v254, 6
	v_readlane_b32 s39, v254, 7
	s_andn2_b64 vcc, exec, s[0:1]
	s_mov_b64 s[0:1], -1
	s_cbranch_vccz .LBB0_1572
	s_waitcnt vmcnt(0)
	s_waitcnt lgkmcnt(0)
	s_barrier
	s_mov_b64 s[2:3], exec
	v_readlane_b32 s0, v254, 3
	v_readlane_b32 s1, v254, 4
	s_and_b64 s[0:1], s[2:3], s[0:1]
	s_mov_b64 exec, s[0:1]
	s_cbranch_execz .LBB0_1571
	s_add_i32 s40, 0, 0x20160
	v_mov_b32_e32 v1, s40
	s_waitcnt vmcnt(0) expcnt(0) lgkmcnt(0)
	ds_read_b32 v4, v1
	v_readlane_b32 s0, v254, 34
	s_waitcnt lgkmcnt(0)
	v_cmp_ne_u32_e32 vcc, 0, v4
	v_mov_b32_e32 v1, s0
	ds_read_b32 v2, v1
	s_cbranch_vccnz .LBB0_1542
	v_readlane_b32 s0, v254, 0
	v_readlane_b32 s1, v254, 1
	s_load_dwordx2 s[6:7], s[0:1], 0x4
	s_add_u32 s0, s36, 0x1000
	s_addc_u32 s1, s37, 0
	s_add_u32 s4, s36, 0x1100
	s_addc_u32 s5, s37, 0
	v_readlane_b32 s8, v254, 2
	s_waitcnt lgkmcnt(0)
	s_mul_i32 s28, s6, s8
	s_add_u32 s6, s36, 0x1200
	s_mul_i32 s28, s28, s7
	s_addc_u32 s7, s37, 0
	s_add_u32 s8, s36, 0x1300
	s_addc_u32 s9, s37, 0
	s_mov_b32 s29, 1
	s_mov_b64 s[10:11], 0
	s_branch .LBB0_1532

; #define PG8_BAR __builtin_amdgcn_s_barrier()
; template <class Epi, class Sched, bool ALIGN_EPI = false, bool SP2 = false, bool F8 = false, bool BTILED = false, bool ATILED = false>
; __device__ __forceinline__ void gemm_phase(PG8_LAS unsigned char* lds, const Gemm g, const Sched& S, const Epi& E) {
;     ...
;         if constexpr (!Epi::AFTER_DRAIN) { E(acc, cur, wr, wc, fr, fq); S.done(cur); }
;         if (!has_next) break;
; #pragma unroll
;         for (int a = 0; a < 2; ++a)
; #pragma unroll
;             for (int b = 0; b < 2; ++b)
; #pragma unroll
;                 for (int m = 0; m < 4; ++m)
; #pragma unroll
;                     for (int n = 0; n < 2; ++n) acc[a][b][m][n] = (f32x4){0.f, 0.f, 0.f, 0.f};
;         cur = nxt; cA = nA; cB = nB; ++ui;
;         if constexpr (ALIGN_EPI) { if (wr == 1) PG8_BAR; }
;     }
.LBB0_1653:
	s_andn2_b64 vcc, exec, s[2:3]
	s_mov_b32 s43, s42
	s_mov_b32 s18, s10
	s_mov_b64 s[2:3], s[16:17]
	s_mov_b64 s[20:21], s[14:15]
	s_cbranch_vccz .LBB0_1663
	s_cmp_lg_u32 s54, 0
	s_cbranch_scc1 .Lh_skip
	s_add_u32 s100, s41, s88
	s_and_b32 s100, s100, 1
	s_cmp_lg_u32 s100, 0
	s_cbranch_scc1 .Lh_skip0
	v_writelane_b32 v222, s0, 0
	v_writelane_b32 v222, s1, 1
	v_writelane_b32 v222, s2, 2
	v_writelane_b32 v222, s3, 3
	v_writelane_b32 v222, s4, 4
	v_writelane_b32 v222, s5, 5
	v_writelane_b32 v222, s6, 6
	v_writelane_b32 v222, s7, 7
	v_writelane_b32 v222, s8, 8
	v_writelane_b32 v222, s9, 9
	v_writelane_b32 v222, s10, 10
	v_writelane_b32 v222, s11, 11
	v_writelane_b32 v222, s12, 12
	v_writelane_b32 v222, s13, 13
	v_writelane_b32 v222, s14, 14
	v_writelane_b32 v222, s15, 15
	v_writelane_b32 v222, s16, 16
	v_writelane_b32 v222, s17, 17
	v_writelane_b32 v222, s18, 18
	v_writelane_b32 v222, s19, 19
	v_writelane_b32 v222, s20, 20
	v_writelane_b32 v222, s21, 21
	v_writelane_b32 v222, s22, 22
	v_writelane_b32 v222, s23, 23
	v_writelane_b32 v222, s89, 24
	v_writelane_b32 v222, s94, 25
	v_mov_b32_e32 v223, v1
	v_mov_b32_e32 v221, v182
	s_mov_b32 s100, 0x1234
	s_branch .Lfl_entry
.Lh_return:
	v_readlane_b32 s0, v222, 0
	v_readlane_b32 s1, v222, 1
	v_readlane_b32 s2, v222, 2
	v_readlane_b32 s3, v222, 3
	v_readlane_b32 s4, v222, 4
	v_readlane_b32 s5, v222, 5
	v_readlane_b32 s6, v222, 6
	v_readlane_b32 s7, v222, 7
	v_readlane_b32 s8, v222, 8
	v_readlane_b32 s9, v222, 9
	v_readlane_b32 s10, v222, 10
	v_readlane_b32 s11, v222, 11
	v_readlane_b32 s12, v222, 12
	v_readlane_b32 s13, v222, 13
	v_readlane_b32 s14, v222, 14
	v_readlane_b32 s15, v222, 15
	v_readlane_b32 s16, v222, 16
	v_readlane_b32 s17, v222, 17
	v_readlane_b32 s18, v222, 18
	v_readlane_b32 s19, v222, 19
	v_readlane_b32 s20, v222, 20
	v_readlane_b32 s21, v222, 21
	v_readlane_b32 s22, v222, 22
	v_readlane_b32 s23, v222, 23
	v_readlane_b32 s89, v222, 24
	v_readlane_b32 s94, v222, 25
	v_mov_b32_e32 v1, v223
	v_mov_b32_e32 v182, v221
	s_nop 3
.Lh_skip0:
	s_mov_b32 s100, 0
.Lh_skip:
.LBB0_1654:
	s_add_i32 s41, s41, 1
	s_mul_i32 s4, s41, s39
	s_mul_hi_u32 s5, s41, s24
	s_add_i32 s5, s5, s4
	s_mul_i32 s4, s41, s24
	s_add_u32 s14, s4, s25
	s_addc_u32 s15, s5, s40
	v_mov_b64_e32 v[2:3], 0xb00
	v_cmp_lt_i64_e64 s[4:5], s[14:15], v[2:3]
	v_mov_b64_e32 v[2:3], 0xaff
	v_cmp_gt_i64_e32 vcc, s[14:15], v[2:3]
	s_cbranch_vccnz .LBB0_1656
	s_mul_hi_i32 s10, s14, 0x2e8ba2e9
	s_lshr_b32 s11, s10, 31
	s_ashr_i32 s10, s10, 5
	s_add_i32 s11, s10, s11
	s_mul_i32 s10, s11, 0xb0
	s_sub_i32 s12, s14, s10
	s_lshl_b32 s10, s11, 3
	s_and_b32 s13, s12, 7
	s_ashr_i32 s42, s12, 3
	s_mul_i32 s11, s11, 22
	s_or_b32 s10, s13, s10
	s_add_i32 s12, s11, s42
